# diff attention (original L/T roles): row-sum adds of the softmax moved behind the next barrier in both L and T paths; plus earlier load-batching edits
# baseline (speedup 1.0000x reference)
; #define WSTEP_T(t, PAR) do { const bool more_ = (t) + 1 < NT; if (more_) WLOADK(((t) + 1) * KVBLK, 1 - PAR); if ((t) > 0) WPV(1 - PAR); WBARN(more_, 1); if (more_) WLOADV(((t) + 1) * KVBLK, 1 - PAR); WQKSM(t, PAR); WBARN(more_, 4); } while (0)
; #define WSTEP_T(t, PAR) do { const bool more_ = (t) + 1 < NT; if (more_) WLOADK((t) + 1, 1 - PAR); if ((t) > 0) WPV(1 - PAR); WBARN(more_, 1); if (more_) WLOADV((t) + 1, 1 - PAR); WQKSM(t, PAR); WBARN(more_, 2); } while (0)
; __device__ __forceinline__ void finishSM8(f32x16& p0, f32x16& p1, float alpha, float& l_reg, i32x8& pa) {
;     for (int r = 0; r < 16; ++r) p1[r] = __builtin_amdgcn_exp2f(p1[r]);
;     float ps;
;     { float s0 = p0[0] + p0[1], s1 = p0[2] + p0[3], s2 = p1[0] + p1[1], s3 = p1[2] + p1[3];
; #pragma unroll
;       for (int r = 4; r < 16; r += 4) { s0 += p0[r]; s0 += p0[r + 1]; s1 += p0[r + 2]; s1 += p0[r + 3]; s2 += p1[r]; s2 += p1[r + 1]; s3 += p1[r + 2]; s3 += p1[r + 3]; }
;       ps = (s0 + s1) + (s2 + s3); }
;     { auto rr = __builtin_amdgcn_permlane32_swap(__float_as_uint(ps), __float_as_uint(ps), false, false);
;       ps = __uint_as_float(rr[0]) + __uint_as_float(rr[1]); }
;     l_reg = l_reg * alpha + ps;
; template <class Epi>
; __device__ __forceinline__ void block_wide8(const BlockRef& cur, const bf16* V2, int skv, char* lds, Seam& S, const Epi& E) {
;     ...
;         for (int t = 0; t < NT; t += 2) { WSTEP_T(t, 0); WSTEP_T(t + 1, 1); }
.LBB0_1205:
	s_barrier
	v_add_f32_e32 v146, v147, v150
	v_add_f32_e32 v166, v10, v12
	v_add_f32_e32 v167, v151, v165
	v_add_f32_e32 v168, v152, v160
	v_add_f32_e32 v146, v148, v146
	v_add_f32_e32 v166, v14, v166
	v_add_f32_e32 v167, v163, v167
	v_add_f32_e32 v168, v161, v168
	v_add_f32_e32 v146, v149, v146
	v_add_f32_e32 v166, v15, v166
	v_add_f32_e32 v167, v164, v167
	v_add_f32_e32 v168, v162, v168
	v_add_f32_e32 v146, v11, v146
	v_add_f32_e32 v166, v4, v166
	v_add_f32_e32 v167, v153, v167
	v_add_f32_e32 v168, v17, v168
	v_add_f32_e32 v146, v13, v146
	v_add_f32_e32 v166, v5, v166
	v_add_f32_e32 v167, v159, v167
	v_add_f32_e32 v168, v154, v168
	v_add_f32_e32 v146, v8, v146
	v_add_f32_e32 v166, v6, v166
	v_add_f32_e32 v167, v157, v167
	v_add_f32_e32 v168, v155, v168
	v_add_f32_e32 v146, v9, v146
	v_add_f32_e32 v166, v7, v166
	v_add_f32_e32 v167, v158, v167
	v_add_f32_e32 v168, v156, v168
	v_add_f32_e32 v146, v166, v146
	v_add_f32_e32 v166, v167, v168
	v_add_f32_e32 v166, v166, v146
	v_mov_b32_e32 v167, v166
	s_nop 1
	v_permlane32_swap_b32_e32 v166, v167
	v_mov_b32_e32 v146, 0
	v_cvt_pk_fp8_f32 v146, v147, v150
	v_mov_b32_e32 v150, 0
	v_cvt_pk_fp8_f32 v150, v151, v165
	v_mov_b32_e32 v147, 0
	v_cvt_pk_fp8_f32 v147, v148, v149
	v_mov_b32_e32 v151, 0
	v_cvt_pk_fp8_f32 v150, v152, v160 op_sel:[0,0,1]
	v_mov_b32_e32 v152, 0
	v_mov_b32_e32 v148, 0
	v_cvt_pk_fp8_f32 v152, v153, v159
	v_mov_b32_e32 v149, 0
	v_mov_b32_e32 v153, 0
	v_cvt_pk_fp8_f32 v151, v163, v164
	v_cvt_pk_fp8_f32 v148, v11, v13
	v_cvt_pk_fp8_f32 v149, v8, v9
	v_cvt_pk_fp8_f32 v153, v157, v158
	v_cvt_pk_fp8_f32 v146, v10, v12 op_sel:[0,0,1]
	v_cvt_pk_fp8_f32 v147, v14, v15 op_sel:[0,0,1]
	v_cvt_pk_fp8_f32 v151, v161, v162 op_sel:[0,0,1]
	v_cvt_pk_fp8_f32 v148, v4, v5 op_sel:[0,0,1]
	v_cvt_pk_fp8_f32 v152, v17, v154 op_sel:[0,0,1]
	v_cvt_pk_fp8_f32 v149, v6, v7 op_sel:[0,0,1]
	v_cvt_pk_fp8_f32 v153, v155, v156 op_sel:[0,0,1]
	v_add_f32_e32 v4, v242, v243
	v_fmac_f32_e32 v4, v215, v2
	v_add_f32_e32 v215, v166, v167
	s_add_u32 s90, s90, 0x4000
	v_fmac_f32_e32 v215, v4, v16
	s_addc_u32 s91, s91, 0
	s_add_i32 s73, s73, 2
	v_add_u32_e32 v240, 0xffffff80, v240
	s_addk_i32 s78, 0x80
	s_and_b64 vcc, exec, s[70:71]
	s_cbranch_vccnz .LBB0_1245

;     ...
;     constexpr float SCL = SCALE / (float)(1 << SH), C2 = 1.4426950408889634f * SCL;
;     if (__builtin_expect(__all((pmax - m_reg) * SCL <= (float)THRI), 1)) { mn = m_reg; alpha = 1.f; }
;     else { mn = fmaxf(m_reg, pmax); alpha = __builtin_amdgcn_exp2f((m_reg - mn) * C2); m_reg = mn; }
;     const float mnL = dead ? -__builtin_inff() : -mn * C2 + (float)PSH;
;     for (int r = 0; r < 16; ++r) p0[r] = fmaf(p0[r], C2, mnL); for (int r = 0; r < 16; ++r) p1[r] = fmaf(p1[r], C2, mnL);
;     for (int r = 0; r < 16; ++r) p0[r] = __builtin_amdgcn_exp2f(p0[r]);
; }
; __device__ __forceinline__ void finishSM(f32x16& p0, f32x16& p1, float alpha, float& l_reg, bf16x8& pa0, bf16x8& pa1, bf16x8& pa2, bf16x8& pa3) {
;     for (int r = 0; r < 16; ++r) p1[r] = __builtin_amdgcn_exp2f(p1[r]);
.LBB0_1219:
	v_cndmask_b32_e64 v241, v242, v241, s[6:7]
	v_fmamk_f32 v194, v241, 0xba0293ee, v1
	v_fmamk_f32 v4, v162, 0x3a0293ee, v194
	v_fmamk_f32 v5, v163, 0x3a0293ee, v194
	v_fmamk_f32 v6, v164, 0x3a0293ee, v194
	v_fmamk_f32 v7, v165, 0x3a0293ee, v194
	v_fmamk_f32 v164, v172, 0x3a0293ee, v194
	v_fmamk_f32 v165, v173, 0x3a0293ee, v194
	v_fmamk_f32 v146, v146, 0x3a0293ee, v194
	v_fmamk_f32 v147, v147, 0x3a0293ee, v194
	v_fmamk_f32 v148, v148, 0x3a0293ee, v194
	v_fmamk_f32 v149, v149, 0x3a0293ee, v194
	v_fmamk_f32 v8, v166, 0x3a0293ee, v194
	v_fmamk_f32 v11, v168, 0x3a0293ee, v194
	v_fmamk_f32 v13, v169, 0x3a0293ee, v194
	v_fmamk_f32 v162, v170, 0x3a0293ee, v194
	v_fmamk_f32 v168, v176, 0x3a0293ee, v194
	v_fmamk_f32 v169, v177, 0x3a0293ee, v194
	v_fmamk_f32 v170, v150, 0x3a0293ee, v194
	v_fmamk_f32 v152, v152, 0x3a0293ee, v194
	v_fmamk_f32 v172, v154, 0x3a0293ee, v194
	v_fmamk_f32 v173, v155, 0x3a0293ee, v194
	v_fmamk_f32 v176, v158, 0x3a0293ee, v194
	v_fmamk_f32 v177, v159, 0x3a0293ee, v194
	v_exp_f32_e32 v154, v4
	v_exp_f32_e32 v155, v5
	v_exp_f32_e32 v10, v6
	v_exp_f32_e32 v12, v7
	v_exp_f32_e32 v4, v164
	v_exp_f32_e32 v5, v165
	v_exp_f32_e32 v164, v146
	v_exp_f32_e32 v165, v147
	v_exp_f32_e32 v158, v148
	v_exp_f32_e32 v159, v149
	v_fmamk_f32 v9, v167, 0x3a0293ee, v194
	v_fmamk_f32 v163, v171, 0x3a0293ee, v194
	v_fmamk_f32 v171, v151, 0x3a0293ee, v194
	v_fmamk_f32 v153, v153, 0x3a0293ee, v194
	v_fmamk_f32 v195, v160, 0x3a0293ee, v194
	v_exp_f32_e32 v150, v8
	v_exp_f32_e32 v14, v11
	v_exp_f32_e32 v11, v162
	v_exp_f32_e32 v162, v170
	v_exp_f32_e32 v160, v152
	v_fmamk_f32 v166, v174, 0x3a0293ee, v194
	v_fmamk_f32 v167, v175, 0x3a0293ee, v194
	v_fmamk_f32 v174, v156, 0x3a0293ee, v194
	v_fmamk_f32 v175, v157, 0x3a0293ee, v194
	v_fmac_f32_e32 v194, 0x3a0293ee, v161
	v_exp_f32_e32 v151, v9
	v_exp_f32_e32 v15, v13
	v_exp_f32_e32 v13, v163
	v_exp_f32_e32 v163, v171
	v_exp_f32_e32 v161, v153
	v_exp_f32_e32 v156, v172
	v_exp_f32_e32 v146, v174
	v_exp_f32_e32 v8, v166
	v_exp_f32_e32 v9, v167
	v_exp_f32_e32 v6, v168
	v_exp_f32_e32 v7, v169
	v_exp_f32_e32 v157, v173
	v_exp_f32_e32 v147, v175
	v_exp_f32_e32 v152, v176
	v_exp_f32_e32 v148, v195
	v_exp_f32_e32 v153, v177
	v_exp_f32_e32 v149, v194
	s_setprio 0
	s_mov_b64 s[6:7], -1
	s_and_b64 vcc, exec, s[70:71]
	s_cbranch_vccz .LBB0_1221
	s_waitcnt vmcnt(0) lgkmcnt(0)
	s_mov_b64 s[6:7], 0

; __device__ __forceinline__ void finishSM8(f32x16& p0, f32x16& p1, float alpha, float& l_reg, i32x8& pa) {
;     for (int r = 0; r < 16; ++r) p1[r] = __builtin_amdgcn_exp2f(p1[r]);
;     float ps;
;     { float s0 = p0[0] + p0[1], s1 = p0[2] + p0[3], s2 = p1[0] + p1[1], s3 = p1[2] + p1[3];
; #pragma unroll
;       for (int r = 4; r < 16; r += 4) { s0 += p0[r]; s0 += p0[r + 1]; s1 += p0[r + 2]; s1 += p0[r + 3]; s2 += p1[r]; s2 += p1[r + 1]; s3 += p1[r + 2]; s3 += p1[r + 3]; }
;       ps = (s0 + s1) + (s2 + s3); }
;     { auto rr = __builtin_amdgcn_permlane32_swap(__float_as_uint(ps), __float_as_uint(ps), false, false);
;       ps = __uint_as_float(rr[0]) + __uint_as_float(rr[1]); }
;     l_reg = l_reg * alpha + ps;
; #pragma unroll
;     for (int d = 0; d < 4; ++d) { int w0 = 0, w1 = 0;
;         w0 = __builtin_amdgcn_cvt_pk_fp8_f32(p0[4 * d], p0[4 * d + 1], w0, false); w0 = __builtin_amdgcn_cvt_pk_fp8_f32(p0[4 * d + 2], p0[4 * d + 3], w0, true);
;         w1 = __builtin_amdgcn_cvt_pk_fp8_f32(p1[4 * d], p1[4 * d + 1], w1, false); w1 = __builtin_amdgcn_cvt_pk_fp8_f32(p1[4 * d + 2], p1[4 * d + 3], w1, true);
;         pa[d] = w0; pa[4 + d] = w1; }
.LBB0_1225:
	v_add_f32_e32 v166, v154, v155
	v_add_f32_e32 v167, v10, v12
	v_add_f32_e32 v168, v164, v165
	v_add_f32_e32 v169, v158, v159
	v_add_f32_e32 v166, v150, v166
	v_add_f32_e32 v167, v14, v167
	v_add_f32_e32 v168, v162, v168
	v_add_f32_e32 v169, v160, v169
	v_add_f32_e32 v166, v151, v166
	v_add_f32_e32 v167, v15, v167
	v_add_f32_e32 v168, v163, v168
	v_add_f32_e32 v169, v161, v169
	v_add_f32_e32 v166, v11, v166
	v_add_f32_e32 v167, v4, v167
	v_add_f32_e32 v168, v156, v168
	v_add_f32_e32 v169, v146, v169
	v_add_f32_e32 v166, v13, v166
	v_add_f32_e32 v167, v5, v167
	v_add_f32_e32 v168, v157, v168
	v_add_f32_e32 v169, v147, v169
	v_add_f32_e32 v166, v8, v166
	v_add_f32_e32 v167, v6, v167
	v_add_f32_e32 v168, v152, v168
	v_add_f32_e32 v169, v148, v169
	v_add_f32_e32 v166, v9, v166
	v_add_f32_e32 v167, v7, v167
	v_add_f32_e32 v168, v153, v168
	v_add_f32_e32 v169, v149, v169
	v_add_f32_e32 v166, v167, v166
	v_add_f32_e32 v167, v168, v169
	v_add_f32_e32 v242, v167, v166
	v_mov_b32_e32 v243, v242
	s_nop 1
	v_permlane32_swap_b32_e32 v242, v243
	v_mov_b32_e32 v166, 0
	v_mov_b32_e32 v170, 0
	v_mov_b32_e32 v167, 0
	v_mov_b32_e32 v171, 0
	v_mov_b32_e32 v168, 0
	v_mov_b32_e32 v172, 0
	v_mov_b32_e32 v169, 0
	v_mov_b32_e32 v173, 0
	v_cvt_pk_fp8_f32 v166, v154, v155
	v_cvt_pk_fp8_f32 v170, v164, v165
	v_cvt_pk_fp8_f32 v167, v150, v151
	v_cvt_pk_fp8_f32 v171, v162, v163
	v_cvt_pk_fp8_f32 v168, v11, v13
	v_cvt_pk_fp8_f32 v172, v156, v157
	v_cvt_pk_fp8_f32 v169, v8, v9
	v_cvt_pk_fp8_f32 v173, v152, v153
	v_cvt_pk_fp8_f32 v166, v10, v12 op_sel:[0,0,1]
	v_cvt_pk_fp8_f32 v170, v158, v159 op_sel:[0,0,1]
	v_cvt_pk_fp8_f32 v167, v14, v15 op_sel:[0,0,1]
	v_cvt_pk_fp8_f32 v171, v160, v161 op_sel:[0,0,1]
	v_cvt_pk_fp8_f32 v168, v4, v5 op_sel:[0,0,1]
	v_cvt_pk_fp8_f32 v172, v146, v147 op_sel:[0,0,1]
	v_cvt_pk_fp8_f32 v169, v6, v7 op_sel:[0,0,1]
	v_cvt_pk_fp8_f32 v173, v148, v149 op_sel:[0,0,1]
	ds_read_b128 v[4:7], v203
	ds_read_b128 v[146:149], v203 offset:2048
	ds_read_b128 v[8:11], v214
	ds_read_b128 v[150:153], v214 offset:2048
	s_waitcnt lgkmcnt(0)
	v_mfma_f32_32x32x64_f8f6f4 v[130:145], v[166:173], v[4:11], v[130:145]
	ds_read_b128 v[4:7], v203 offset:4096
	ds_read_b128 v[8:11], v214 offset:4096
	v_mfma_f32_32x32x64_f8f6f4 v[114:129], v[166:173], v[146:153], v[114:129]
	ds_read_b128 v[146:149], v203 offset:6144
	ds_read_b128 v[150:153], v214 offset:6144
	s_waitcnt lgkmcnt(0)
	v_mfma_f32_32x32x64_f8f6f4 v[98:113], v[166:173], v[4:11], v[98:113]
	ds_read_b128 v[4:7], v203 offset:16384
	ds_read_b128 v[8:11], v214 offset:16384
	v_mfma_f32_32x32x64_f8f6f4 v[82:97], v[166:173], v[146:153], v[82:97]
	ds_read_b128 v[146:149], v203 offset:18432
	ds_read_b128 v[150:153], v214 offset:18432
	s_waitcnt lgkmcnt(0)
	v_mfma_f32_32x32x64_f8f6f4 v[66:81], v[166:173], v[4:11], v[66:81]
	ds_read_b128 v[4:7], v203 offset:20480
	ds_read_b128 v[8:11], v214 offset:20480
	v_mfma_f32_32x32x64_f8f6f4 v[50:65], v[166:173], v[146:153], v[50:65]
	ds_read_b128 v[146:149], v203 offset:22528
	ds_read_b128 v[150:153], v214 offset:22528
	s_waitcnt lgkmcnt(0)
	v_mfma_f32_32x32x64_f8f6f4 v[34:49], v[166:173], v[4:11], v[34:49]
	v_mfma_f32_32x32x64_f8f6f4 v[18:33], v[166:173], v[146:153], v[18:33]
	s_nop 15
	s_nop 15
	s_mov_b64 s[8:9], -1
	s_and_b64 vcc, exec, s[70:71]
	s_cbranch_vccz .LBB0_1227
	s_waitcnt vmcnt(0) lgkmcnt(0)
	s_mov_b64 s[8:9], 0

;     ...
;     constexpr float SCL = SCALE / (float)(1 << SH), C2 = 1.4426950408889634f * SCL;
;     if (__builtin_expect(__all((pmax - m_reg) * SCL <= (float)THRI), 1)) { mn = m_reg; alpha = 1.f; }
;     else { mn = fmaxf(m_reg, pmax); alpha = __builtin_amdgcn_exp2f((m_reg - mn) * C2); m_reg = mn; }
;     const float mnL = dead ? -__builtin_inff() : -mn * C2 + (float)PSH;
;     for (int r = 0; r < 16; ++r) p0[r] = fmaf(p0[r], C2, mnL); for (int r = 0; r < 16; ++r) p1[r] = fmaf(p1[r], C2, mnL);
;     for (int r = 0; r < 16; ++r) p0[r] = __builtin_amdgcn_exp2f(p0[r]);
; }
; __device__ __forceinline__ void finishSM(f32x16& p0, f32x16& p1, float alpha, float& l_reg, bf16x8& pa0, bf16x8& pa1, bf16x8& pa2, bf16x8& pa3) {
;     for (int r = 0; r < 16; ++r) p1[r] = __builtin_amdgcn_exp2f(p1[r]);
.LBB0_1237:
	v_cndmask_b32_e64 v241, v17, v241, s[6:7]
	v_fmamk_f32 v194, v241, 0xba0293ee, v1
	v_fmamk_f32 v4, v162, 0x3a0293ee, v194
	v_fmamk_f32 v5, v163, 0x3a0293ee, v194
	v_fmamk_f32 v6, v164, 0x3a0293ee, v194
	v_fmamk_f32 v7, v165, 0x3a0293ee, v194
	v_fmamk_f32 v8, v166, 0x3a0293ee, v194
	v_fmamk_f32 v13, v169, 0x3a0293ee, v194
	v_fmamk_f32 v17, v170, 0x3a0293ee, v194
	v_fmamk_f32 v162, v171, 0x3a0293ee, v194
	v_fmamk_f32 v165, v174, 0x3a0293ee, v194
	v_fmamk_f32 v146, v146, 0x3a0293ee, v194
	v_fmamk_f32 v169, v147, 0x3a0293ee, v194
	v_fmamk_f32 v170, v148, 0x3a0293ee, v194
	v_fmamk_f32 v171, v149, 0x3a0293ee, v194
	v_fmamk_f32 v9, v167, 0x3a0293ee, v194
	v_fmamk_f32 v11, v168, 0x3a0293ee, v194
	v_fmamk_f32 v163, v172, 0x3a0293ee, v194
	v_fmamk_f32 v164, v173, 0x3a0293ee, v194
	v_fmamk_f32 v167, v176, 0x3a0293ee, v194
	v_fmamk_f32 v172, v150, 0x3a0293ee, v194
	v_fmamk_f32 v173, v151, 0x3a0293ee, v194
	v_fmamk_f32 v174, v152, 0x3a0293ee, v194
	v_fmamk_f32 v176, v160, 0x3a0293ee, v194
	v_exp_f32_e32 v147, v4
	v_exp_f32_e32 v150, v5
	v_exp_f32_e32 v10, v6
	v_exp_f32_e32 v12, v7
	v_exp_f32_e32 v148, v8
	v_exp_f32_e32 v8, v165
	v_exp_f32_e32 v151, v146
	v_exp_f32_e32 v165, v169
	v_exp_f32_e32 v152, v170
	v_exp_f32_e32 v160, v171
	v_fmamk_f32 v166, v175, 0x3a0293ee, v194
	v_fmamk_f32 v168, v177, 0x3a0293ee, v194
	v_fmamk_f32 v153, v153, 0x3a0293ee, v194
	v_fmamk_f32 v154, v154, 0x3a0293ee, v194
	v_fmamk_f32 v155, v155, 0x3a0293ee, v194
	v_fmamk_f32 v156, v156, 0x3a0293ee, v194
	v_fmamk_f32 v157, v157, 0x3a0293ee, v194
	v_fmamk_f32 v158, v158, 0x3a0293ee, v194
	v_fmamk_f32 v175, v159, 0x3a0293ee, v194
	v_fmac_f32_e32 v194, 0x3a0293ee, v161
	v_exp_f32_e32 v14, v11
	v_exp_f32_e32 v4, v163
	v_exp_f32_e32 v163, v172
	v_exp_f32_e32 v161, v174
	v_exp_f32_e32 v149, v9
	v_exp_f32_e32 v15, v13
	v_exp_f32_e32 v13, v162
	v_exp_f32_e32 v5, v164
	v_exp_f32_e32 v164, v173
	v_exp_f32_e32 v162, v153
	v_exp_f32_e32 v11, v17
	v_exp_f32_e32 v153, v154
	v_exp_f32_e32 v17, v156
	v_exp_f32_e32 v9, v166
	v_exp_f32_e32 v6, v167
	v_exp_f32_e32 v7, v168
	v_exp_f32_e32 v159, v155
	v_exp_f32_e32 v154, v157
	v_exp_f32_e32 v157, v158
	v_exp_f32_e32 v155, v176
	v_exp_f32_e32 v158, v175
	v_exp_f32_e32 v156, v194
	s_setprio 0
	s_mov_b64 s[6:7], -1
	s_and_b64 vcc, exec, s[70:71]
	s_cbranch_vccz .LBB0_1239
	s_waitcnt vmcnt(0) lgkmcnt(0)
	s_mov_b64 s[6:7], 0
